# baseline (speedup 1.0000x reference)
_Z9ssim_mainPKfS0_S0_Pf:
	v_readfirstlane_b32 s29, v0
	s_load_dwordx4 s[4:7], s[0:1], 0x0
	s_load_dwordx4 s[8:11], s[0:1], 0x10
	s_mov_b32 s51, 0x44800000
	s_mov_b32 s38, 0
	s_mov_b32 s39, -1
	s_lshr_b32 s12, s29, 6
	s_and_b32 s13, s2, 7
	s_lshl_b32 s13, s13, 5
	s_lshr_b32 s14, s2, 3
	s_add_u32 s13, s13, s14
	s_lshr_b32 s14, s13, 3
	s_and_b32 s15, s13, 7
	s_lshl_b32 s16, s14, 20
	s_lshl_b32 s17, s15, 17
	s_add_u32 s16, s16, s17
	s_lshl_b32 s17, s12, 8
	s_add_u32 s16, s16, s17
	s_lshl_b32 s27, s12, 2
	s_add_u32 s27, s27, 0x10000
	v_and_b32_e32 v8, 63, v0
	v_and_b32_e32 v169, 15, v0
	v_bfe_u32 v164, v0, 4, 2
	v_lshrrev_b32_e32 v167, 2, v169
	v_lshlrev_b32_e32 v167, 5, v167
	v_and_b32_e32 v168, 1, v169
	v_lshl_or_b32 v167, v168, 4, v167
	v_bfe_u32 v168, v169, 1, 1
	v_lshl_or_b32 v167, v168, 7, v167
	v_lshl_or_b32 v9, v164, 14, v167
	v_and_b32_e32 v168, 1, v164
	v_lshl_or_b32 v23, v168, 14, v167
	v_lshrrev_b32_e32 v168, 1, v164
	v_lshl_or_b32 v23, v168, 13, v23
	v_add_u32_e32 v237, 0x1000, v9
	v_add_u32_e32 v238, 0x2000, v9
	v_add_u32_e32 v239, 0x3000, v9
	v_add_u32_e32 v240, 0x10000, v9
	v_add_u32_e32 v241, 0x11000, v9
	v_add_u32_e32 v242, 0x12000, v9
	v_add_u32_e32 v243, 0x13000, v9
	s_waitcnt lgkmcnt(0)
	s_load_dwordx8 s[40:47], s[8:9], 0x0
	s_load_dwordx2 s[48:49], s[8:9], 0x20
	s_load_dword s50, s[8:9], 0x28
	s_add_u32 s18, s4, s16
	s_addc_u32 s19, s5, 0
	s_add_u32 s20, s6, s16
	s_addc_u32 s21, s7, 0
	global_load_dwordx4 v[36:39], v9, s[18:19] offset:0 sc1 nt
	global_load_dwordx4 v[40:43], v9, s[18:19] offset:2048 sc1 nt
	global_load_dwordx4 v[68:71], v9, s[20:21] offset:0 sc1 nt
	global_load_dwordx4 v[72:75], v9, s[20:21] offset:2048 sc1 nt
	global_load_dwordx4 v[44:47], v237, s[18:19] offset:0 sc1 nt
	global_load_dwordx4 v[48:51], v237, s[18:19] offset:2048 sc1 nt
	global_load_dwordx4 v[76:79], v237, s[20:21] offset:0 sc1 nt
	global_load_dwordx4 v[80:83], v237, s[20:21] offset:2048 sc1 nt
	global_load_dwordx4 v[52:55], v238, s[18:19] offset:0 sc1 nt
	global_load_dwordx4 v[56:59], v238, s[18:19] offset:2048 sc1 nt
	global_load_dwordx4 v[84:87], v238, s[20:21] offset:0 sc1 nt
	global_load_dwordx4 v[88:91], v238, s[20:21] offset:2048 sc1 nt
	global_load_dwordx4 v[60:63], v239, s[18:19] offset:0 sc1 nt
	global_load_dwordx4 v[64:67], v239, s[18:19] offset:2048 sc1 nt
	global_load_dwordx4 v[92:95], v239, s[20:21] offset:0 sc1 nt
	global_load_dwordx4 v[96:99], v239, s[20:21] offset:2048 sc1 nt
	global_load_dwordx4 v[100:103], v240, s[18:19] offset:0 sc1 nt
	global_load_dwordx4 v[104:107], v240, s[18:19] offset:2048 sc1 nt
	global_load_dwordx4 v[132:135], v240, s[20:21] offset:0 sc1 nt
	global_load_dwordx4 v[136:139], v240, s[20:21] offset:2048 sc1 nt
	global_load_dwordx4 v[108:111], v241, s[18:19] offset:0 sc1 nt
	global_load_dwordx4 v[112:115], v241, s[18:19] offset:2048 sc1 nt
	global_load_dwordx4 v[140:143], v241, s[20:21] offset:0 sc1 nt
	global_load_dwordx4 v[144:147], v241, s[20:21] offset:2048 sc1 nt
	global_load_dwordx4 v[116:119], v242, s[18:19] offset:0 sc1 nt
	global_load_dwordx4 v[120:123], v242, s[18:19] offset:2048 sc1 nt
	global_load_dwordx4 v[148:151], v242, s[20:21] offset:0 sc1 nt
	global_load_dwordx4 v[152:155], v242, s[20:21] offset:2048 sc1 nt
	global_load_dwordx4 v[124:127], v243, s[18:19] offset:0 sc1 nt
	global_load_dwordx4 v[128:131], v243, s[18:19] offset:2048 sc1 nt
	global_load_dwordx4 v[156:159], v243, s[20:21] offset:0 sc1 nt
	global_load_dwordx4 v[160:163], v243, s[20:21] offset:2048 sc1 nt
	v_mov_b32_e32 v6, s27
	v_mov_b32_e32 v168, 0
	ds_write_b32 v6, v168 offset:0
	ds_write_b32 v6, v168 offset:32
	ds_write_b32 v6, v168 offset:64
	ds_write_b32 v6, v168 offset:96
	v_lshlrev_b32_e32 v167, 3, v164
	v_xor_b32_e32 v168, 16, v167
	v_sub_u32_e32 v165, v167, v169
	v_sub_u32_e32 v166, v168, v169
	v_add_u32_e32 v172, 0, v165
	v_min_u32_e32 v172, 11, v172
	v_lshlrev_b32_e32 v172, 2, v172
	v_add_u32_e32 v173, 1, v165
	v_min_u32_e32 v173, 11, v173
	v_lshlrev_b32_e32 v173, 2, v173
	v_add_u32_e32 v174, 2, v165
	v_min_u32_e32 v174, 11, v174
	v_lshlrev_b32_e32 v174, 2, v174
	v_add_u32_e32 v175, 3, v165
	v_min_u32_e32 v175, 11, v175
	v_lshlrev_b32_e32 v175, 2, v175
	v_add_u32_e32 v176, 4, v165
	v_min_u32_e32 v176, 11, v176
	v_lshlrev_b32_e32 v176, 2, v176
	v_add_u32_e32 v177, 5, v165
	v_min_u32_e32 v177, 11, v177
	v_lshlrev_b32_e32 v177, 2, v177
	v_add_u32_e32 v178, 6, v165
	v_min_u32_e32 v178, 11, v178
	v_lshlrev_b32_e32 v178, 2, v178
	v_add_u32_e32 v179, 7, v165
	v_min_u32_e32 v179, 11, v179
	v_lshlrev_b32_e32 v179, 2, v179
	v_add_u32_e32 v180, 0, v166
	v_min_u32_e32 v180, 11, v180
	v_lshlrev_b32_e32 v180, 2, v180
	v_add_u32_e32 v181, 1, v166
	v_min_u32_e32 v181, 11, v181
	v_lshlrev_b32_e32 v181, 2, v181
	v_add_u32_e32 v182, 2, v166
	v_min_u32_e32 v182, 11, v182
	v_lshlrev_b32_e32 v182, 2, v182
	v_add_u32_e32 v183, 3, v166
	v_min_u32_e32 v183, 11, v183
	v_lshlrev_b32_e32 v183, 2, v183
	v_add_u32_e32 v184, 4, v166
	v_min_u32_e32 v184, 11, v184
	v_lshlrev_b32_e32 v184, 2, v184
	v_add_u32_e32 v185, 5, v166
	v_min_u32_e32 v185, 11, v185
	v_lshlrev_b32_e32 v185, 2, v185
	v_add_u32_e32 v186, 6, v166
	v_min_u32_e32 v186, 11, v186
	v_lshlrev_b32_e32 v186, 2, v186
	v_add_u32_e32 v187, 7, v166
	v_min_u32_e32 v187, 11, v187
	v_lshlrev_b32_e32 v187, 2, v187
	s_cmp_eq_u32 s15, 7
	s_cselect_b32 s22, 0, 0x20000
	s_add_u32 s84, s18, s22
	s_addc_u32 s85, s19, 0
	s_add_u32 s86, s18, s22
	s_addc_u32 s87, s19, 0
	s_add_u32 s86, s86, 0x1000
	s_addc_u32 s87, s87, 0
	s_add_u32 s88, s20, s22
	s_addc_u32 s89, s21, 0
	s_add_u32 s90, s20, s22
	s_addc_u32 s91, s21, 0
	s_add_u32 s90, s90, 0x1000
	s_addc_u32 s91, s91, 0
	s_waitcnt lgkmcnt(0)
	v_writelane_b32 v171, s40, 0
	v_writelane_b32 v171, s41, 1
	v_writelane_b32 v171, s42, 2
	v_writelane_b32 v171, s43, 3
	v_writelane_b32 v171, s44, 4
	v_writelane_b32 v171, s45, 5
	v_writelane_b32 v171, s46, 6
	v_writelane_b32 v171, s47, 7
	v_writelane_b32 v171, s48, 8
	v_writelane_b32 v171, s49, 9
	v_writelane_b32 v171, s50, 10
	v_writelane_b32 v171, 0, 11
	v_fma_mixlo_f16 v171, v171, s51, 0
	ds_bpermute_b32 v188, v172, v171
	ds_bpermute_b32 v189, v173, v171
	ds_bpermute_b32 v190, v174, v171
	ds_bpermute_b32 v191, v175, v171
	ds_bpermute_b32 v192, v176, v171
	ds_bpermute_b32 v193, v177, v171
	ds_bpermute_b32 v194, v178, v171
	ds_bpermute_b32 v195, v179, v171
	v_mov_b32_e32 v229, 0x44800000
	v_fma_mixlo_f16 v228, s40, v229, 0
	v_cvt_f32_f16_e32 v228, v228
	v_cvt_f64_f32_e32 v[212:213], v228
	v_add_f64 v[212:213], v[212:213], 0
	v_fma_mixlo_f16 v228, s41, v229, 0
	v_cvt_f32_f16_e32 v228, v228
	v_cvt_f64_f32_e32 v[214:215], v228
	v_add_f64 v[212:213], v[212:213], v[214:215]
	v_fma_mixlo_f16 v228, s42, v229, 0
	v_cvt_f32_f16_e32 v228, v228
	v_cvt_f64_f32_e32 v[214:215], v228
	v_add_f64 v[212:213], v[212:213], v[214:215]
	v_fma_mixlo_f16 v228, s43, v229, 0
	v_cvt_f32_f16_e32 v228, v228
	v_cvt_f64_f32_e32 v[214:215], v228
	v_add_f64 v[212:213], v[212:213], v[214:215]
	v_fma_mixlo_f16 v228, s44, v229, 0
	v_cvt_f32_f16_e32 v228, v228
	v_cvt_f64_f32_e32 v[214:215], v228
	v_add_f64 v[212:213], v[212:213], v[214:215]
	v_fma_mixlo_f16 v228, s45, v229, 0
	v_cvt_f32_f16_e32 v228, v228
	v_cvt_f64_f32_e32 v[214:215], v228
	v_add_f64 v[212:213], v[212:213], v[214:215]
	v_fma_mixlo_f16 v228, s46, v229, 0
	v_cvt_f32_f16_e32 v228, v228
	v_cvt_f64_f32_e32 v[214:215], v228
	v_add_f64 v[212:213], v[212:213], v[214:215]
	v_fma_mixlo_f16 v228, s47, v229, 0
	v_cvt_f32_f16_e32 v228, v228
	v_cvt_f64_f32_e32 v[214:215], v228
	v_add_f64 v[212:213], v[212:213], v[214:215]
	v_fma_mixlo_f16 v228, s48, v229, 0
	v_cvt_f32_f16_e32 v228, v228
	v_cvt_f64_f32_e32 v[214:215], v228
	v_add_f64 v[212:213], v[212:213], v[214:215]
	v_fma_mixlo_f16 v228, s49, v229, 0
	v_cvt_f32_f16_e32 v228, v228
	v_cvt_f64_f32_e32 v[214:215], v228
	v_add_f64 v[212:213], v[212:213], v[214:215]
	v_fma_mixlo_f16 v228, s50, v229, 0
	v_cvt_f32_f16_e32 v228, v228
	v_cvt_f64_f32_e32 v[214:215], v228
	v_add_f64 v[212:213], v[212:213], v[214:215]
	s_waitcnt lgkmcnt(7)
	ds_bpermute_b32 v196, v180, v171
	ds_bpermute_b32 v197, v181, v171
	ds_bpermute_b32 v198, v182, v171
	ds_bpermute_b32 v199, v183, v171
	ds_bpermute_b32 v200, v184, v171
	ds_bpermute_b32 v201, v185, v171
	ds_bpermute_b32 v202, v186, v171
	ds_bpermute_b32 v203, v187, v171
	v_mul_f64 v[212:213], v[212:213], v[212:213]
	v_mul_f64 v[216:217], v[212:213], 0.5
	v_add_f64 v[218:219], v[216:217], v[216:217]
	s_mov_b32 s36, 0xeb1c432d
	s_mov_b32 s37, 0x3f1a36e2
	v_mul_f64 v[220:221], v[212:213], s[36:37]
	v_mul_f64 v[222:223], v[216:217], v[218:219]
	v_fmac_f64_e32 v[222:223], v[212:213], v[220:221]
	v_add_f64 v[224:225], v[212:213], v[212:213]
	s_mov_b32 s36, 0x487fcb92
	s_mov_b32 s37, 0x3f4d7dbf
	v_mul_f64 v[226:227], v[212:213], s[36:37]
	v_cvt_f32_f64_e32 v0, v[226:227]
	v_mov_b32_e32 v1, v0
	v_mov_b32_e32 v2, v0
	v_mov_b32_e32 v3, v0
	v_cvt_f32_f64_e32 v10, v[218:219]
	v_cvt_f32_f64_e32 v11, v[222:223]
	v_cvt_f32_f64_e32 v12, v[212:213]
	v_cvt_f32_f64_e32 v13, v[224:225]
	v_mul_f64 v[226:227], v[212:213], v[226:227]
	v_cvt_f32_f64_e32 v14, v[226:227]
	v_lshlrev_b32_e32 v167, 2, v164
	s_cmp_eq_u32 s12, 0
	s_cselect_b32 s23, 6, 64
	v_add_u32_e32 v168, 0, v167
	v_cmp_gt_u32_e32 vcc, s23, v168
	s_nop 1
	v_cndmask_b32_e64 v15, 0, 1.0, vcc
	v_add_u32_e32 v168, 1, v167
	v_cmp_gt_u32_e32 vcc, s23, v168
	s_nop 1
	v_cndmask_b32_e64 v16, 0, 1.0, vcc
	v_add_u32_e32 v168, 2, v167
	v_cmp_gt_u32_e32 vcc, s23, v168
	s_nop 1
	v_cndmask_b32_e64 v17, 0, 1.0, vcc
	v_add_u32_e32 v168, 3, v167
	v_cmp_gt_u32_e32 vcc, s23, v168
	s_nop 1
	v_cndmask_b32_e64 v18, 0, 1.0, vcc
	v_and_b32_e32 v167, 31, v8
	v_lshlrev_b32_e32 v167, 4, v167
	s_lshl_b32 s24, s12, 11
	s_add_i32 s25, s12, 7
	s_and_b32 s25, s25, 7
	s_lshl_b32 s26, s25, 11
	v_or_b32_e32 v4, s24, v167
	v_or_b32_e32 v5, s26, v167
	s_lshl_b32 s28, s25, 2
	s_add_u32 s28, s28, 0x10000
	v_mov_b32_e32 v7, s28
	v_mov_b32_e32 v19, 0
	v_mov_b32_e32 v20, 0
	v_mov_b32_e32 v21, 0
	v_mov_b32_e32 v22, 0
	s_waitcnt lgkmcnt(0)
	v_cmp_lt_u32_e64 s[32:33], 31, v8
	v_cmp_gt_u32_e64 s[34:35], 32, v8
	v_pack_b32_f16 v24, v188, v189
	v_pack_b32_f16 v25, v190, v191
	v_pack_b32_f16 v26, v192, v193
	v_pack_b32_f16 v27, v194, v195
	v_pack_b32_f16 v167, v196, v197
	v_cndmask_b32_e64 v28, 0, v167, s[32:33]
	v_cndmask_b32_e64 v32, 0, v167, s[34:35]
	v_pack_b32_f16 v167, v198, v199
	v_cndmask_b32_e64 v29, 0, v167, s[32:33]
	v_cndmask_b32_e64 v33, 0, v167, s[34:35]
	v_pack_b32_f16 v167, v200, v201
	v_cndmask_b32_e64 v30, 0, v167, s[32:33]
	v_cndmask_b32_e64 v34, 0, v167, s[34:35]
	v_pack_b32_f16 v167, v202, v203
	v_cndmask_b32_e64 v31, 0, v167, s[32:33]
	v_cndmask_b32_e64 v35, 0, v167, s[34:35]
	s_waitcnt lgkmcnt(0)
	s_cmp_lt_u32 s12, 4
	s_cbranch_scc1 .Lq_noprio
	s_setprio 1
